# projection GEMM q/k epilogue: the xor-16 / xor-32 ds_bpermute hops of each row-block sum replaced by permlane16/32 swaps plus add (same summation tree, f32)
# baseline (speedup 1.0000x reference)
.LBB0_173:
	s_and_b64 vcc, exec, s[8:9]
	s_cbranch_vccz .LBB0_175
	s_lshl_b64 s[4:5], s[38:39], 2
	s_cmp_lt_i32 s96, 2
	s_cselect_b64 vcc, -1, 0
	s_and_b64 s[8:9], vcc, exec
	s_cselect_b32 s9, s12, s14
	s_mov_b32 s23, 0x5c00000
	s_cselect_b32 s8, s13, s15
	s_cselect_b32 s23, s23, 0x7c00000
	s_add_u32 s4, s9, s4
	s_addc_u32 s5, s8, s5
	v_ashrrev_i32_e32 v179, 31, v178
	v_mov_b32_e32 v130, 0x3e38aa3b
	v_lshl_add_u64 v[134:135], v[178:179], 2, s[4:5]
	v_cndmask_b32_e32 v157, 1.0, v130, vcc
	global_load_dwordx4 v[138:141], v[134:135], off offset:16
	global_load_dwordx4 v[142:145], v[134:135], off
	global_load_dwordx4 v[130:133], v[134:135], off offset:144
	s_nop 0
	global_load_dwordx4 v[134:137], v[134:135], off offset:128
	v_cvt_f32_i32_e32 v181, v125
	v_cvt_f32_i32_e32 v180, v124
	v_cvt_f32_i32_e32 v183, v123
	v_cvt_f32_i32_e32 v182, v122
	v_cvt_f32_i32_e32 v191, v115
	v_pk_mul_f32 v[188:189], v[174:175], v[180:181] op_sel_hi:[0,1]
	v_pk_mul_f32 v[180:181], v[188:189], v[188:189]
	v_pk_mul_f32 v[186:187], v[174:175], v[182:183] op_sel_hi:[0,1]
	v_pk_mul_f32 v[182:183], v[186:187], v[186:187]
	v_cvt_f32_i32_e32 v190, v114
	v_pk_mov_b32 v[184:185], v[182:183], v[180:181] op_sel:[1,0]
	v_mov_b32_e32 v183, v181
	v_cvt_f32_i32_e32 v181, v117
	v_cvt_f32_i32_e32 v180, v116
	v_pk_add_f32 v[182:183], v[184:185], v[182:183]
	v_pk_mul_f32 v[190:191], v[174:175], v[190:191] op_sel_hi:[0,1]
	v_pk_add_f32 v[194:195], v[182:183], v[182:183] op_sel_hi:[0,1]
	v_pk_mul_f32 v[196:197], v[174:175], v[180:181] op_sel_hi:[0,1]
	v_pk_mul_f32 v[180:181], v[196:197], v[196:197]
	v_pk_mul_f32 v[182:183], v[190:191], v[190:191]
	v_cvt_f32_i32_e32 v199, v129
	v_pk_mov_b32 v[184:185], v[182:183], v[180:181] op_sel:[1,0]
	v_mov_b32_e32 v183, v181
	v_cvt_f32_i32_e32 v181, v127
	v_cvt_f32_i32_e32 v180, v126
	v_cvt_f32_i32_e32 v198, v128
	v_pk_add_f32 v[182:183], v[184:185], v[182:183]
	v_cvt_f32_i32_e32 v185, v119
	v_pk_add_f32 v[200:201], v[182:183], v[182:183] op_sel_hi:[0,1]
	v_pk_mul_f32 v[202:203], v[174:175], v[180:181] op_sel_hi:[0,1]
	v_cvt_f32_i32_e32 v183, v121
	v_cvt_f32_i32_e32 v182, v120
	v_cvt_f32_i32_e32 v184, v118
	v_mul_f32_e32 v180, v202, v202
	v_pk_mul_f32 v[198:199], v[174:175], v[198:199] op_sel_hi:[0,1]
	v_pk_fma_f32 v[180:181], v[202:203], v[202:203], v[180:181] op_sel_hi:[1,1,0]
	v_and_b32_e32 v161, 64, v234
	v_mul_f32_e32 v180, v198, v198
	v_pk_fma_f32 v[204:205], v[198:199], v[198:199], v[180:181] op_sel_hi:[1,1,0]
	v_pk_mul_f32 v[182:183], v[174:175], v[182:183] op_sel_hi:[0,1]
	v_pk_mul_f32 v[184:185], v[174:175], v[184:185] op_sel_hi:[0,1]
	v_xor_b32_e32 v159, 16, v234
	v_add_u32_e32 v161, 64, v161
	v_mul_f32_e32 v180, v184, v184
	v_mul_f32_e32 v204, v185, v185
	v_mul_f32_e32 v194, v182, v182
	v_mul_f32_e32 v200, v183, v183
	v_cmp_lt_i32_e32 vcc, v159, v161
	v_pk_add_f32 v[180:181], v[180:181], v[204:205]
	v_pk_add_f32 v[194:195], v[194:195], v[200:201]
	v_cndmask_b32_e32 v159, v234, v159, vcc
	v_pk_add_f32 v[180:181], v[180:181], v[194:195]
	v_lshlrev_b32_e32 v159, 2, v159
	v_add_f32_e32 v163, v180, v181

	v_xor_b32_e32 v171, 32, v234
	v_cmp_lt_i32_e32 vcc, v171, v161
	s_add_u32 s4, s10, s23
	s_addc_u32 s5, s11, 0
	v_cndmask_b32_e32 v161, v234, v171, vcc
	v_lshlrev_b32_e32 v161, 2, v161
	s_waitcnt lgkmcnt(0)
	v_mov_b32_e32 v167, v163
	s_nop 1
	v_permlane16_swap_b32_e32 v163, v167
	s_nop 0
	v_add_f32_e32 v163, v163, v167

	s_lshl_b32 s8, s96, 9
	s_and_b32 s8, s8, 0x200
	s_add_u32 s4, s4, s8
	s_addc_u32 s5, s5, 0
	s_waitcnt lgkmcnt(0)
	v_mov_b32_e32 v167, v163
	s_nop 1
	v_permlane32_swap_b32_e32 v163, v167
	s_nop 0
	v_add_f32_e32 v163, v163, v167
	v_fmamk_f32 v163, v163, 0x3c800000, v235
	v_rsq_f32_e32 v163, v163
	s_add_u32 s4, s4, s63
	s_addc_u32 s5, s5, 0
	v_lshl_add_u64 v[180:181], v[178:179], 1, s[4:5]
	v_mul_f32_e32 v194, v157, v163
	v_pk_mul_f32 v[186:187], v[186:187], v[194:195] op_sel_hi:[1,0]
	v_pk_mul_f32 v[188:189], v[188:189], v[194:195] op_sel_hi:[1,0]
	v_pk_mul_f32 v[190:191], v[190:191], v[194:195] op_sel_hi:[1,0]
	v_pk_mul_f32 v[196:197], v[196:197], v[194:195] op_sel_hi:[1,0]
	v_lshlrev_b64 v[178:179], 10, v[168:169]
	s_waitcnt vmcnt(2)
	v_pk_mul_f32 v[188:189], v[144:145], v[188:189]
	v_pk_mul_f32 v[186:187], v[142:143], v[186:187]
	v_pk_mul_f32 v[196:197], v[140:141], v[196:197]
	v_pk_mul_f32 v[190:191], v[138:139], v[190:191]
	v_lshl_add_u64 v[178:179], v[180:181], 0, v[178:179]
	v_cvt_pk_bf16_f32 v186, v186, v187
	v_cvt_pk_bf16_f32 v187, v188, v189
	v_cvt_pk_bf16_f32 v188, v190, v191
	v_cvt_pk_bf16_f32 v189, v196, v197
	global_store_dwordx4 v[178:179], v[186:189], off
	v_pk_mul_f32 v[196:197], v[198:199], v[194:195] op_sel_hi:[1,0]
	v_pk_mul_f32 v[190:191], v[202:203], v[194:195] op_sel_hi:[1,0]
	v_cvt_f32_i32_e32 v187, v109
	v_cvt_f32_i32_e32 v189, v107
	v_cvt_f32_i32_e32 v188, v106
	v_cvt_f32_i32_e32 v186, v108
	v_cvt_f32_i32_e32 v205, v99
	v_cvt_f32_i32_e32 v204, v98
	v_pk_mul_f32 v[198:199], v[172:173], v[188:189] op_sel_hi:[0,1]
	v_pk_mul_f32 v[200:201], v[172:173], v[186:187] op_sel_hi:[0,1]
	v_pk_mul_f32 v[186:187], v[200:201], v[200:201]
	v_pk_mul_f32 v[188:189], v[198:199], v[198:199]
	v_pk_mul_f32 v[204:205], v[172:173], v[204:205] op_sel_hi:[0,1]
	v_pk_mov_b32 v[202:203], v[188:189], v[186:187] op_sel:[1,0]
	v_mov_b32_e32 v189, v187
	v_cvt_f32_i32_e32 v187, v101
	v_cvt_f32_i32_e32 v186, v100
	v_pk_add_f32 v[188:189], v[202:203], v[188:189]
	v_cvt_f32_i32_e32 v211, v113
	v_pk_add_f32 v[202:203], v[188:189], v[188:189] op_sel_hi:[0,1]
	v_pk_mul_f32 v[206:207], v[172:173], v[186:187] op_sel_hi:[0,1]
	v_pk_mul_f32 v[186:187], v[206:207], v[206:207]
	v_pk_mul_f32 v[188:189], v[204:205], v[204:205]
	v_cvt_f32_i32_e32 v210, v112
	v_pk_mov_b32 v[208:209], v[188:189], v[186:187] op_sel:[1,0]
	v_mov_b32_e32 v189, v187
	v_cvt_f32_i32_e32 v187, v111
	v_cvt_f32_i32_e32 v186, v110
	v_pk_add_f32 v[188:189], v[208:209], v[188:189]
	v_pk_mul_f32 v[210:211], v[172:173], v[210:211] op_sel_hi:[0,1]
	v_pk_add_f32 v[208:209], v[188:189], v[188:189] op_sel_hi:[0,1]
	v_pk_mul_f32 v[212:213], v[172:173], v[186:187] op_sel_hi:[0,1]
	v_mul_f32_e32 v186, v212, v212
	v_pk_fma_f32 v[214:215], v[212:213], v[212:213], v[186:187] op_sel_hi:[1,1,0]
	v_cvt_f32_i32_e32 v189, v103
	v_cvt_f32_i32_e32 v187, v105
	v_cvt_f32_i32_e32 v186, v104
	v_cvt_f32_i32_e32 v188, v102
	v_mul_f32_e32 v202, v210, v210
	v_pk_fma_f32 v[216:217], v[210:211], v[210:211], v[202:203] op_sel_hi:[1,1,0]
	v_pk_mul_f32 v[186:187], v[172:173], v[186:187] op_sel_hi:[0,1]
	v_pk_mul_f32 v[188:189], v[172:173], v[188:189] op_sel_hi:[0,1]
	v_mul_f32_e32 v214, v188, v188
	v_mul_f32_e32 v216, v189, v189
	v_mul_f32_e32 v202, v186, v186
	v_mul_f32_e32 v208, v187, v187
	v_pk_add_f32 v[214:215], v[214:215], v[216:217]
	v_pk_add_f32 v[202:203], v[202:203], v[208:209]
	v_pk_mul_f32 v[184:185], v[184:185], v[194:195] op_sel_hi:[1,0]
	v_pk_add_f32 v[202:203], v[214:215], v[202:203]
	v_pk_mul_f32 v[182:183], v[182:183], v[194:195] op_sel_hi:[1,0]
	v_add_f32_e32 v163, v202, v203

	s_waitcnt vmcnt(1)
	v_pk_mul_f32 v[196:197], v[136:137], v[196:197]
	v_pk_mul_f32 v[190:191], v[134:135], v[190:191]
	v_pk_mul_f32 v[194:195], v[132:133], v[182:183]
	v_pk_mul_f32 v[184:185], v[130:131], v[184:185]
	s_waitcnt lgkmcnt(0)
	v_mov_b32_e32 v167, v163
	s_nop 1
	v_permlane16_swap_b32_e32 v163, v167
	s_nop 0
	v_add_f32_e32 v163, v163, v167

	v_cvt_pk_bf16_f32 v182, v190, v191
	v_cvt_pk_bf16_f32 v183, v196, v197
	v_cvt_pk_bf16_f32 v184, v184, v185
	v_cvt_pk_bf16_f32 v185, v194, v195
	s_waitcnt lgkmcnt(0)
	v_mov_b32_e32 v167, v163
	s_nop 1
	v_permlane32_swap_b32_e32 v163, v167
	s_nop 0
	v_add_f32_e32 v163, v163, v167
	v_fmamk_f32 v163, v163, 0x3c800000, v235
	v_rsq_f32_e32 v163, v163
	global_store_dwordx4 v[178:179], v[182:185], off offset:64
	s_mov_b64 s[4:5], 0x24000
	v_mul_f32_e32 v202, v157, v163
	v_or_b32_e32 v182, 16, v168
	v_ashrrev_i32_e32 v183, 31, v182
	v_lshlrev_b64 v[182:183], 10, v[182:183]
	v_lshl_add_u64 v[184:185], v[180:181], 0, v[182:183]
	v_pk_mul_f32 v[182:183], v[198:199], v[202:203] op_sel_hi:[1,0]
	v_pk_mul_f32 v[190:191], v[200:201], v[202:203] op_sel_hi:[1,0]
	v_pk_mul_f32 v[182:183], v[142:143], v[182:183]
	v_pk_mul_f32 v[190:191], v[144:145], v[190:191]
	v_pk_mul_f32 v[194:195], v[204:205], v[202:203] op_sel_hi:[1,0]
	v_pk_mul_f32 v[196:197], v[206:207], v[202:203] op_sel_hi:[1,0]
	v_cvt_f32_i32_e32 v207, v83
	v_pk_mul_f32 v[198:199], v[140:141], v[196:197]
	v_pk_mul_f32 v[196:197], v[138:139], v[194:195]
	v_cvt_pk_bf16_f32 v194, v182, v183
	v_cvt_pk_bf16_f32 v195, v190, v191
	v_cvt_f32_i32_e32 v183, v93
	v_cvt_f32_i32_e32 v191, v91
	v_cvt_f32_i32_e32 v190, v90
	v_cvt_f32_i32_e32 v182, v92
	v_cvt_pk_bf16_f32 v196, v196, v197
	v_cvt_pk_bf16_f32 v197, v198, v199
	v_pk_mul_f32 v[198:199], v[170:171], v[190:191] op_sel_hi:[0,1]
	v_pk_mul_f32 v[200:201], v[170:171], v[182:183] op_sel_hi:[0,1]
	v_pk_mul_f32 v[182:183], v[200:201], v[200:201]
	v_pk_mul_f32 v[190:191], v[198:199], v[198:199]
	v_cvt_f32_i32_e32 v206, v82
	v_pk_mov_b32 v[204:205], v[190:191], v[182:183] op_sel:[1,0]
	v_mov_b32_e32 v191, v183
	v_cvt_f32_i32_e32 v183, v85
	v_cvt_f32_i32_e32 v182, v84
	v_pk_add_f32 v[190:191], v[204:205], v[190:191]
	v_pk_mul_f32 v[206:207], v[170:171], v[206:207] op_sel_hi:[0,1]
	v_pk_add_f32 v[204:205], v[190:191], v[190:191] op_sel_hi:[0,1]
	v_pk_mul_f32 v[208:209], v[170:171], v[182:183] op_sel_hi:[0,1]
	v_pk_mul_f32 v[182:183], v[208:209], v[208:209]
	v_pk_mul_f32 v[190:191], v[206:207], v[206:207]
	global_store_dwordx4 v[184:185], v[194:197], off
	v_pk_mul_f32 v[188:189], v[188:189], v[202:203] op_sel_hi:[1,0]
	v_pk_mul_f32 v[186:187], v[186:187], v[202:203] op_sel_hi:[1,0]
	v_pk_mul_f32 v[196:197], v[210:211], v[202:203] op_sel_hi:[1,0]
	v_pk_mov_b32 v[210:211], v[190:191], v[182:183] op_sel:[1,0]
	v_mov_b32_e32 v191, v183
	v_cvt_f32_i32_e32 v183, v95
	v_cvt_f32_i32_e32 v182, v94
	v_pk_mul_f32 v[194:195], v[212:213], v[202:203] op_sel_hi:[1,0]
	v_cvt_f32_i32_e32 v213, v97
	v_cvt_f32_i32_e32 v212, v96
	v_pk_mul_f32 v[214:215], v[170:171], v[182:183] op_sel_hi:[0,1]
	v_pk_add_f32 v[190:191], v[210:211], v[190:191]
	v_mul_f32_e32 v182, v214, v214
	v_pk_add_f32 v[210:211], v[190:191], v[190:191] op_sel_hi:[0,1]
	v_pk_fma_f32 v[216:217], v[214:215], v[214:215], v[182:183] op_sel_hi:[1,1,0]
	v_cvt_f32_i32_e32 v191, v87
	v_cvt_f32_i32_e32 v183, v89
	v_cvt_f32_i32_e32 v182, v88
	v_cvt_f32_i32_e32 v190, v86
	v_pk_mul_f32 v[212:213], v[170:171], v[212:213] op_sel_hi:[0,1]
	v_mul_f32_e32 v204, v212, v212
	v_pk_fma_f32 v[218:219], v[212:213], v[212:213], v[204:205] op_sel_hi:[1,1,0]
	v_pk_mul_f32 v[182:183], v[170:171], v[182:183] op_sel_hi:[0,1]
	v_pk_mul_f32 v[190:191], v[170:171], v[190:191] op_sel_hi:[0,1]
	v_mul_f32_e32 v216, v190, v190
	v_mul_f32_e32 v218, v191, v191
	v_mul_f32_e32 v204, v182, v182
	v_mul_f32_e32 v210, v183, v183
	v_pk_add_f32 v[216:217], v[216:217], v[218:219]
	v_pk_add_f32 v[204:205], v[204:205], v[210:211]
	v_pk_mul_f32 v[196:197], v[136:137], v[196:197]
	v_pk_add_f32 v[204:205], v[216:217], v[204:205]
	v_pk_mul_f32 v[194:195], v[134:135], v[194:195]
	v_add_f32_e32 v163, v204, v205

	v_pk_mul_f32 v[202:203], v[132:133], v[186:187]
	v_pk_mul_f32 v[188:189], v[130:131], v[188:189]
	v_cvt_pk_bf16_f32 v186, v194, v195
	v_cvt_pk_bf16_f32 v187, v196, v197
	s_waitcnt lgkmcnt(0)
	v_mov_b32_e32 v167, v163
	s_nop 1
	v_permlane16_swap_b32_e32 v163, v167
	s_nop 0
	v_add_f32_e32 v163, v163, v167

	v_cvt_pk_bf16_f32 v188, v188, v189
	v_cvt_pk_bf16_f32 v189, v202, v203
	global_store_dwordx4 v[184:185], v[186:189], off offset:64
	v_or_b32_e32 v184, 32, v168
	s_waitcnt lgkmcnt(0)
	v_mov_b32_e32 v167, v163
	s_nop 1
	v_permlane32_swap_b32_e32 v163, v167
	s_nop 0
	v_add_f32_e32 v163, v163, v167
	v_fmamk_f32 v163, v163, 0x3c800000, v235
	v_rsq_f32_e32 v163, v163
	v_ashrrev_i32_e32 v185, 31, v184
	v_lshlrev_b64 v[184:185], 10, v[184:185]
	v_lshl_add_u64 v[188:189], v[180:181], 0, v[184:185]
	v_mul_f32_e32 v194, v157, v163
	v_pk_mul_f32 v[184:185], v[198:199], v[194:195] op_sel_hi:[1,0]
	v_pk_mul_f32 v[186:187], v[200:201], v[194:195] op_sel_hi:[1,0]
	v_pk_mul_f32 v[196:197], v[206:207], v[194:195] op_sel_hi:[1,0]
	v_pk_mul_f32 v[198:199], v[208:209], v[194:195] op_sel_hi:[1,0]
	v_pk_mul_f32 v[186:187], v[144:145], v[186:187]
	v_pk_mul_f32 v[184:185], v[142:143], v[184:185]
	v_pk_mul_f32 v[198:199], v[140:141], v[198:199]
	v_pk_mul_f32 v[196:197], v[138:139], v[196:197]
	v_cvt_pk_bf16_f32 v184, v184, v185
	v_cvt_pk_bf16_f32 v185, v186, v187
	v_cvt_pk_bf16_f32 v186, v196, v197
	v_cvt_pk_bf16_f32 v187, v198, v199
	global_store_dwordx4 v[188:189], v[184:187], off
	v_cvt_f32_i32_e32 v207, v67
	v_cvt_f32_i32_e32 v206, v66
	v_cvt_f32_i32_e32 v185, v77
	v_cvt_f32_i32_e32 v187, v75
	v_cvt_f32_i32_e32 v186, v74
	v_cvt_f32_i32_e32 v184, v76
	v_pk_mul_f32 v[206:207], v[166:167], v[206:207] op_sel_hi:[0,1]
	v_pk_mul_f32 v[196:197], v[214:215], v[194:195] op_sel_hi:[1,0]
	v_pk_mul_f32 v[200:201], v[166:167], v[186:187] op_sel_hi:[0,1]
	v_pk_mul_f32 v[202:203], v[166:167], v[184:185] op_sel_hi:[0,1]
	v_pk_mul_f32 v[184:185], v[202:203], v[202:203]
	v_pk_mul_f32 v[186:187], v[200:201], v[200:201]
	v_pk_mul_f32 v[198:199], v[212:213], v[194:195] op_sel_hi:[1,0]
	v_pk_mov_b32 v[204:205], v[186:187], v[184:185] op_sel:[1,0]
	v_mov_b32_e32 v187, v185
	v_cvt_f32_i32_e32 v185, v69
	v_cvt_f32_i32_e32 v184, v68
	v_pk_add_f32 v[186:187], v[204:205], v[186:187]
	v_cvt_f32_i32_e32 v213, v81
	v_pk_add_f32 v[204:205], v[186:187], v[186:187] op_sel_hi:[0,1]
	v_pk_mul_f32 v[208:209], v[166:167], v[184:185] op_sel_hi:[0,1]
	v_pk_mul_f32 v[184:185], v[208:209], v[208:209]
	v_pk_mul_f32 v[186:187], v[206:207], v[206:207]
	v_cvt_f32_i32_e32 v212, v80
	v_pk_mov_b32 v[210:211], v[186:187], v[184:185] op_sel:[1,0]
	v_mov_b32_e32 v187, v185
	v_cvt_f32_i32_e32 v185, v79
	v_cvt_f32_i32_e32 v184, v78
	v_pk_add_f32 v[186:187], v[210:211], v[186:187]
	v_pk_mul_f32 v[212:213], v[166:167], v[212:213] op_sel_hi:[0,1]
	v_pk_add_f32 v[210:211], v[186:187], v[186:187] op_sel_hi:[0,1]
	v_pk_mul_f32 v[214:215], v[166:167], v[184:185] op_sel_hi:[0,1]
	v_mul_f32_e32 v184, v214, v214
	v_pk_fma_f32 v[216:217], v[214:215], v[214:215], v[184:185] op_sel_hi:[1,1,0]
	v_cvt_f32_i32_e32 v187, v71
	v_cvt_f32_i32_e32 v185, v73
	v_cvt_f32_i32_e32 v184, v72
	v_cvt_f32_i32_e32 v186, v70
	v_mul_f32_e32 v204, v212, v212
	v_pk_fma_f32 v[218:219], v[212:213], v[212:213], v[204:205] op_sel_hi:[1,1,0]
	v_pk_mul_f32 v[184:185], v[166:167], v[184:185] op_sel_hi:[0,1]
	v_pk_mul_f32 v[186:187], v[166:167], v[186:187] op_sel_hi:[0,1]
	v_mul_f32_e32 v216, v186, v186
	v_mul_f32_e32 v218, v187, v187
	v_mul_f32_e32 v204, v184, v184
	v_mul_f32_e32 v210, v185, v185
	v_pk_add_f32 v[216:217], v[216:217], v[218:219]
	v_pk_add_f32 v[204:205], v[204:205], v[210:211]
	v_pk_mul_f32 v[182:183], v[182:183], v[194:195] op_sel_hi:[1,0]
	v_pk_add_f32 v[204:205], v[216:217], v[204:205]
	v_pk_mul_f32 v[196:197], v[134:135], v[196:197]
	v_add_f32_e32 v163, v204, v205

	v_pk_mul_f32 v[182:183], v[132:133], v[182:183]
	v_pk_mul_f32 v[190:191], v[190:191], v[194:195] op_sel_hi:[1,0]
	v_cvt_pk_bf16_f32 v194, v196, v197
	v_cvt_pk_bf16_f32 v197, v182, v183
	s_waitcnt lgkmcnt(0)
	v_mov_b32_e32 v167, v163
	s_nop 1
	v_permlane16_swap_b32_e32 v163, v167
	s_nop 0
	v_add_f32_e32 v163, v163, v167

	v_or_b32_e32 v182, 48, v168
	v_pk_mul_f32 v[198:199], v[136:137], v[198:199]
	v_pk_mul_f32 v[190:191], v[130:131], v[190:191]
	v_ashrrev_i32_e32 v183, 31, v182
	s_waitcnt lgkmcnt(0)
	v_mov_b32_e32 v167, v163
	s_nop 1
	v_permlane32_swap_b32_e32 v163, v167
	s_nop 0
	v_add_f32_e32 v163, v163, v167
	v_fmamk_f32 v163, v163, 0x3c800000, v235
	v_rsq_f32_e32 v163, v163
	v_cvt_pk_bf16_f32 v195, v198, v199
	v_cvt_pk_bf16_f32 v196, v190, v191
	v_lshlrev_b64 v[182:183], 10, v[182:183]
	v_mul_f32_e32 v198, v157, v163
	global_store_dwordx4 v[188:189], v[194:197], off offset:64
	v_lshl_add_u64 v[190:191], v[180:181], 0, v[182:183]
	v_pk_mul_f32 v[182:183], v[200:201], v[198:199] op_sel_hi:[1,0]
	v_pk_mul_f32 v[188:189], v[202:203], v[198:199] op_sel_hi:[1,0]
	v_pk_mul_f32 v[182:183], v[142:143], v[182:183]
	v_pk_mul_f32 v[188:189], v[144:145], v[188:189]
	v_pk_mul_f32 v[194:195], v[206:207], v[198:199] op_sel_hi:[1,0]
	v_pk_mul_f32 v[196:197], v[208:209], v[198:199] op_sel_hi:[1,0]
	v_cvt_f32_i32_e32 v207, v51
	v_pk_mul_f32 v[200:201], v[140:141], v[196:197]
	v_pk_mul_f32 v[196:197], v[138:139], v[194:195]
	v_cvt_pk_bf16_f32 v194, v182, v183
	v_cvt_pk_bf16_f32 v195, v188, v189
	v_cvt_f32_i32_e32 v183, v61
	v_cvt_f32_i32_e32 v189, v59
	v_cvt_f32_i32_e32 v188, v58
	v_cvt_f32_i32_e32 v182, v60
	v_cvt_pk_bf16_f32 v196, v196, v197
	v_cvt_pk_bf16_f32 v197, v200, v201
	v_pk_mul_f32 v[200:201], v[162:163], v[188:189] op_sel_hi:[0,1]
	v_pk_mul_f32 v[202:203], v[162:163], v[182:183] op_sel_hi:[0,1]
	v_pk_mul_f32 v[182:183], v[202:203], v[202:203]
	v_pk_mul_f32 v[188:189], v[200:201], v[200:201]
	v_cvt_f32_i32_e32 v206, v50
	v_pk_mov_b32 v[204:205], v[188:189], v[182:183] op_sel:[1,0]
	v_mov_b32_e32 v189, v183
	v_cvt_f32_i32_e32 v183, v53
	v_cvt_f32_i32_e32 v182, v52
	v_pk_add_f32 v[188:189], v[204:205], v[188:189]
	v_pk_mul_f32 v[206:207], v[162:163], v[206:207] op_sel_hi:[0,1]
	v_pk_add_f32 v[204:205], v[188:189], v[188:189] op_sel_hi:[0,1]
	v_pk_mul_f32 v[208:209], v[162:163], v[182:183] op_sel_hi:[0,1]
	v_pk_mul_f32 v[182:183], v[208:209], v[208:209]
	v_pk_mul_f32 v[188:189], v[206:207], v[206:207]
	global_store_dwordx4 v[190:191], v[194:197], off
	v_pk_mov_b32 v[210:211], v[188:189], v[182:183] op_sel:[1,0]
	v_mov_b32_e32 v189, v183
	v_cvt_f32_i32_e32 v183, v63
	v_cvt_f32_i32_e32 v182, v62
	v_pk_mul_f32 v[194:195], v[214:215], v[198:199] op_sel_hi:[1,0]
	v_pk_mul_f32 v[196:197], v[212:213], v[198:199] op_sel_hi:[1,0]
	v_cvt_f32_i32_e32 v213, v65
	v_cvt_f32_i32_e32 v212, v64
	v_pk_mul_f32 v[214:215], v[162:163], v[182:183] op_sel_hi:[0,1]
	v_pk_add_f32 v[188:189], v[210:211], v[188:189]
	v_mul_f32_e32 v182, v214, v214
	v_pk_add_f32 v[210:211], v[188:189], v[188:189] op_sel_hi:[0,1]
	v_pk_fma_f32 v[216:217], v[214:215], v[214:215], v[182:183] op_sel_hi:[1,1,0]
	v_cvt_f32_i32_e32 v189, v55
	v_cvt_f32_i32_e32 v183, v57
	v_cvt_f32_i32_e32 v182, v56
	v_cvt_f32_i32_e32 v188, v54
	v_pk_mul_f32 v[212:213], v[162:163], v[212:213] op_sel_hi:[0,1]
	v_mul_f32_e32 v204, v212, v212
	v_pk_fma_f32 v[218:219], v[212:213], v[212:213], v[204:205] op_sel_hi:[1,1,0]
	v_pk_mul_f32 v[182:183], v[162:163], v[182:183] op_sel_hi:[0,1]
	v_pk_mul_f32 v[188:189], v[162:163], v[188:189] op_sel_hi:[0,1]
	v_mul_f32_e32 v216, v188, v188
	v_mul_f32_e32 v218, v189, v189
	v_mul_f32_e32 v204, v182, v182
	v_mul_f32_e32 v210, v183, v183
	v_pk_add_f32 v[216:217], v[216:217], v[218:219]
	v_pk_add_f32 v[204:205], v[204:205], v[210:211]
	v_pk_mul_f32 v[186:187], v[186:187], v[198:199] op_sel_hi:[1,0]
	v_pk_add_f32 v[204:205], v[216:217], v[204:205]
	v_pk_mul_f32 v[184:185], v[184:185], v[198:199] op_sel_hi:[1,0]
	v_add_f32_e32 v163, v204, v205

	v_pk_mul_f32 v[196:197], v[136:137], v[196:197]
	v_pk_mul_f32 v[194:195], v[134:135], v[194:195]
	v_pk_mul_f32 v[198:199], v[132:133], v[184:185]
	v_pk_mul_f32 v[186:187], v[130:131], v[186:187]
	s_waitcnt lgkmcnt(0)
	v_mov_b32_e32 v167, v163
	s_nop 1
	v_permlane16_swap_b32_e32 v163, v167
	s_nop 0
	v_add_f32_e32 v163, v163, v167

	v_cvt_pk_bf16_f32 v184, v194, v195
	v_cvt_pk_bf16_f32 v185, v196, v197
	v_cvt_pk_bf16_f32 v186, v186, v187
	v_cvt_pk_bf16_f32 v187, v198, v199
	s_waitcnt lgkmcnt(0)
	v_mov_b32_e32 v167, v163
	s_nop 1
	v_permlane32_swap_b32_e32 v163, v167
	s_nop 0
	v_add_f32_e32 v163, v163, v167
	v_fmamk_f32 v163, v163, 0x3c800000, v235
	v_rsq_f32_e32 v163, v163
	global_store_dwordx4 v[190:191], v[184:187], off offset:64
	v_cvt_f32_i32_e32 v205, v35
	v_cvt_f32_i32_e32 v204, v34
	v_mul_f32_e32 v190, v157, v163
	v_lshlrev_b64 v[184:185], 10, v[164:165]
	v_lshl_add_u64 v[186:187], v[180:181], 0, v[184:185]
	v_pk_mul_f32 v[180:181], v[200:201], v[190:191] op_sel_hi:[1,0]
	v_pk_mul_f32 v[184:185], v[202:203], v[190:191] op_sel_hi:[1,0]
	v_pk_mul_f32 v[180:181], v[142:143], v[180:181]
	v_pk_mul_f32 v[184:185], v[144:145], v[184:185]
	v_pk_mul_f32 v[194:195], v[206:207], v[190:191] op_sel_hi:[1,0]
	v_pk_mul_f32 v[196:197], v[208:209], v[190:191] op_sel_hi:[1,0]
	v_pk_mul_f32 v[204:205], v[160:161], v[204:205] op_sel_hi:[0,1]
	v_pk_mul_f32 v[198:199], v[140:141], v[196:197]
	v_pk_mul_f32 v[196:197], v[138:139], v[194:195]
	v_cvt_pk_bf16_f32 v194, v180, v181
	v_cvt_pk_bf16_f32 v195, v184, v185
	v_cvt_f32_i32_e32 v181, v45
	v_cvt_f32_i32_e32 v185, v43
	v_cvt_f32_i32_e32 v184, v42
	v_cvt_f32_i32_e32 v180, v44
	v_cvt_pk_bf16_f32 v196, v196, v197
	v_cvt_pk_bf16_f32 v197, v198, v199
	v_pk_mul_f32 v[198:199], v[160:161], v[184:185] op_sel_hi:[0,1]
	v_pk_mul_f32 v[200:201], v[160:161], v[180:181] op_sel_hi:[0,1]
	v_pk_mul_f32 v[180:181], v[200:201], v[200:201]
	v_pk_mul_f32 v[184:185], v[198:199], v[198:199]
	global_store_dwordx4 v[186:187], v[194:197], off
	v_pk_mov_b32 v[202:203], v[184:185], v[180:181] op_sel:[1,0]
	v_mov_b32_e32 v185, v181
	v_cvt_f32_i32_e32 v181, v37
	v_cvt_f32_i32_e32 v180, v36
	v_pk_add_f32 v[184:185], v[202:203], v[184:185]
	v_pk_mul_f32 v[196:197], v[212:213], v[190:191] op_sel_hi:[1,0]
	v_pk_add_f32 v[202:203], v[184:185], v[184:185] op_sel_hi:[0,1]
	v_pk_mul_f32 v[206:207], v[160:161], v[180:181] op_sel_hi:[0,1]
	v_pk_mul_f32 v[180:181], v[206:207], v[206:207]
	v_pk_mul_f32 v[184:185], v[204:205], v[204:205]
	v_cvt_f32_i32_e32 v211, v49
	v_pk_mov_b32 v[208:209], v[184:185], v[180:181] op_sel:[1,0]
	v_mov_b32_e32 v185, v181
	v_cvt_f32_i32_e32 v181, v47
	v_cvt_f32_i32_e32 v180, v46
	v_cvt_f32_i32_e32 v210, v48
	v_pk_add_f32 v[184:185], v[208:209], v[184:185]
	v_pk_mul_f32 v[194:195], v[214:215], v[190:191] op_sel_hi:[1,0]
	v_pk_mul_f32 v[212:213], v[160:161], v[180:181] op_sel_hi:[0,1]
	v_mul_f32_e32 v180, v212, v212
	v_pk_add_f32 v[208:209], v[184:185], v[184:185] op_sel_hi:[0,1]
	v_pk_fma_f32 v[214:215], v[212:213], v[212:213], v[180:181] op_sel_hi:[1,1,0]
	v_cvt_f32_i32_e32 v185, v39
	v_cvt_f32_i32_e32 v181, v41
	v_cvt_f32_i32_e32 v180, v40
	v_cvt_f32_i32_e32 v184, v38
	v_pk_mul_f32 v[210:211], v[160:161], v[210:211] op_sel_hi:[0,1]
	v_mul_f32_e32 v202, v210, v210
	v_pk_fma_f32 v[216:217], v[210:211], v[210:211], v[202:203] op_sel_hi:[1,1,0]
	v_pk_mul_f32 v[180:181], v[160:161], v[180:181] op_sel_hi:[0,1]
	v_pk_mul_f32 v[184:185], v[160:161], v[184:185] op_sel_hi:[0,1]
	v_mul_f32_e32 v214, v184, v184
	v_mul_f32_e32 v216, v185, v185
	v_mul_f32_e32 v202, v180, v180
	v_mul_f32_e32 v208, v181, v181
	v_pk_add_f32 v[214:215], v[214:215], v[216:217]
	v_pk_add_f32 v[202:203], v[202:203], v[208:209]
	v_pk_mul_f32 v[188:189], v[188:189], v[190:191] op_sel_hi:[1,0]
	v_pk_add_f32 v[202:203], v[214:215], v[202:203]
	v_pk_mul_f32 v[182:183], v[182:183], v[190:191] op_sel_hi:[1,0]
	v_add_f32_e32 v163, v202, v203

	v_pk_mul_f32 v[196:197], v[136:137], v[196:197]
	v_pk_mul_f32 v[194:195], v[134:135], v[194:195]
	v_pk_mul_f32 v[182:183], v[132:133], v[182:183]
	v_pk_mul_f32 v[190:191], v[130:131], v[188:189]
	s_waitcnt lgkmcnt(0)
	v_mov_b32_e32 v167, v163
	s_nop 1
	v_permlane16_swap_b32_e32 v163, v167
	s_nop 0
	v_add_f32_e32 v163, v163, v167

	v_cvt_pk_bf16_f32 v188, v194, v195
	v_cvt_pk_bf16_f32 v189, v196, v197
	v_cvt_pk_bf16_f32 v190, v190, v191
	v_cvt_pk_bf16_f32 v191, v182, v183
	s_waitcnt lgkmcnt(0)
	v_mov_b32_e32 v167, v163
	s_nop 1
	v_permlane32_swap_b32_e32 v163, v167
	s_nop 0
	v_add_f32_e32 v163, v163, v167
	v_fmamk_f32 v163, v163, 0x3c800000, v235
	v_rsq_f32_e32 v163, v163
	global_store_dwordx4 v[186:187], v[188:191], off offset:64
	s_nop 1
	v_mul_f32_e32 v190, v157, v163
	v_pk_mul_f32 v[182:183], v[198:199], v[190:191] op_sel_hi:[1,0]
	v_lshl_add_u64 v[188:189], v[178:179], 0, s[4:5]
	v_pk_mul_f32 v[186:187], v[200:201], v[190:191] op_sel_hi:[1,0]
	v_pk_mul_f32 v[182:183], v[142:143], v[182:183]
	v_pk_mul_f32 v[194:195], v[204:205], v[190:191] op_sel_hi:[1,0]
	v_pk_mul_f32 v[196:197], v[206:207], v[190:191] op_sel_hi:[1,0]
	s_mov_b32 s4, 0x24000
	v_pk_mul_f32 v[186:187], v[144:145], v[186:187]
	v_pk_mul_f32 v[198:199], v[140:141], v[196:197]
	v_pk_mul_f32 v[196:197], v[138:139], v[194:195]
	v_cvt_pk_bf16_f32 v194, v182, v183
	v_add_co_u32_e32 v182, vcc, s4, v178
	v_cvt_pk_bf16_f32 v195, v186, v187
	v_cvt_pk_bf16_f32 v196, v196, v197
	v_cvt_pk_bf16_f32 v197, v198, v199
	v_addc_co_u32_e32 v183, vcc, 0, v179, vcc
	global_store_dwordx4 v[182:183], v[194:197], off
	v_cvt_f32_i32_e32 v183, v33
	v_cvt_f32_i32_e32 v187, v31
	v_cvt_f32_i32_e32 v186, v30
	v_cvt_f32_i32_e32 v182, v32
	v_cvt_f32_i32_e32 v205, v19
	v_cvt_f32_i32_e32 v204, v18
	v_pk_mul_f32 v[198:199], v[158:159], v[186:187] op_sel_hi:[0,1]
	v_pk_mul_f32 v[200:201], v[158:159], v[182:183] op_sel_hi:[0,1]
	v_pk_mul_f32 v[182:183], v[200:201], v[200:201]
	v_pk_mul_f32 v[186:187], v[198:199], v[198:199]
	v_pk_mul_f32 v[204:205], v[158:159], v[204:205] op_sel_hi:[0,1]
	v_pk_mov_b32 v[202:203], v[186:187], v[182:183] op_sel:[1,0]
	v_mov_b32_e32 v187, v183
	v_cvt_f32_i32_e32 v183, v21
	v_cvt_f32_i32_e32 v182, v20
	v_pk_add_f32 v[186:187], v[202:203], v[186:187]
	v_pk_mul_f32 v[194:195], v[212:213], v[190:191] op_sel_hi:[1,0]
	v_pk_add_f32 v[202:203], v[186:187], v[186:187] op_sel_hi:[0,1]
	v_pk_mul_f32 v[206:207], v[158:159], v[182:183] op_sel_hi:[0,1]
	v_pk_mul_f32 v[182:183], v[206:207], v[206:207]
	v_pk_mul_f32 v[186:187], v[204:205], v[204:205]
	v_pk_mul_f32 v[196:197], v[210:211], v[190:191] op_sel_hi:[1,0]
	v_pk_mov_b32 v[208:209], v[186:187], v[182:183] op_sel:[1,0]
	v_mov_b32_e32 v187, v183
	v_cvt_f32_i32_e32 v183, v27
	v_cvt_f32_i32_e32 v182, v26
	v_cvt_f32_i32_e32 v211, v29
	v_cvt_f32_i32_e32 v210, v28
	v_pk_add_f32 v[186:187], v[208:209], v[186:187]
	v_pk_mul_f32 v[212:213], v[158:159], v[182:183] op_sel_hi:[0,1]
	v_mul_f32_e32 v182, v212, v212
	v_pk_add_f32 v[208:209], v[186:187], v[186:187] op_sel_hi:[0,1]
	v_pk_fma_f32 v[214:215], v[212:213], v[212:213], v[182:183] op_sel_hi:[1,1,0]
	v_cvt_f32_i32_e32 v187, v23
	v_cvt_f32_i32_e32 v183, v25
	v_cvt_f32_i32_e32 v182, v24
	v_cvt_f32_i32_e32 v186, v22
	v_pk_mul_f32 v[210:211], v[158:159], v[210:211] op_sel_hi:[0,1]
	v_mul_f32_e32 v202, v210, v210
	v_pk_fma_f32 v[216:217], v[210:211], v[210:211], v[202:203] op_sel_hi:[1,1,0]
	v_pk_mul_f32 v[182:183], v[158:159], v[182:183] op_sel_hi:[0,1]
	v_pk_mul_f32 v[186:187], v[158:159], v[186:187] op_sel_hi:[0,1]
	v_mul_f32_e32 v214, v186, v186
	v_mul_f32_e32 v216, v187, v187
	v_mul_f32_e32 v202, v182, v182
	v_mul_f32_e32 v208, v183, v183
	v_pk_add_f32 v[214:215], v[214:215], v[216:217]
	v_pk_add_f32 v[202:203], v[202:203], v[208:209]
	v_pk_mul_f32 v[184:185], v[184:185], v[190:191] op_sel_hi:[1,0]
	v_pk_add_f32 v[202:203], v[214:215], v[202:203]
	v_pk_mul_f32 v[180:181], v[180:181], v[190:191] op_sel_hi:[1,0]
	v_add_f32_e32 v163, v202, v203

	v_pk_mul_f32 v[196:197], v[136:137], v[196:197]
	v_pk_mul_f32 v[194:195], v[134:135], v[194:195]
	v_pk_mul_f32 v[180:181], v[132:133], v[180:181]
	v_pk_mul_f32 v[184:185], v[130:131], v[184:185]
	s_waitcnt lgkmcnt(0)
	v_mov_b32_e32 v167, v163
	s_nop 1
	v_permlane16_swap_b32_e32 v163, v167
	s_nop 0
	v_add_f32_e32 v163, v163, v167

	v_cvt_pk_bf16_f32 v194, v194, v195
	v_cvt_pk_bf16_f32 v195, v196, v197
	v_cvt_pk_bf16_f32 v196, v184, v185
	v_cvt_pk_bf16_f32 v197, v180, v181
	s_waitcnt lgkmcnt(0)
	v_mov_b32_e32 v167, v163
	s_nop 1
	v_permlane32_swap_b32_e32 v163, v167
	s_nop 0
	v_add_f32_e32 v163, v163, v167
	v_fmamk_f32 v163, v163, 0x3c800000, v235
	v_rsq_f32_e32 v163, v163
	global_store_dwordx4 v[188:189], v[194:197], off offset:64
	s_mov_b64 s[4:5], 0x28000
	v_lshl_add_u64 v[180:181], v[178:179], 0, s[4:5]
	v_mul_f32_e32 v184, v157, v163
	v_pk_mul_f32 v[188:189], v[198:199], v[184:185] op_sel_hi:[1,0]
	v_pk_mul_f32 v[190:191], v[200:201], v[184:185] op_sel_hi:[1,0]
	v_pk_mul_f32 v[194:195], v[204:205], v[184:185] op_sel_hi:[1,0]
	v_pk_mul_f32 v[190:191], v[144:145], v[190:191]
	v_pk_mul_f32 v[188:189], v[142:143], v[188:189]
	v_pk_mul_f32 v[196:197], v[206:207], v[184:185] op_sel_hi:[1,0]
	v_pk_mul_f32 v[194:195], v[138:139], v[194:195]
	s_mov_b32 s4, 0x28000
	v_pk_mul_f32 v[196:197], v[140:141], v[196:197]
	v_cvt_pk_bf16_f32 v188, v188, v189
	v_cvt_pk_bf16_f32 v189, v190, v191
	v_cvt_pk_bf16_f32 v190, v194, v195
	v_add_co_u32_e32 v194, vcc, s4, v178
	v_cvt_pk_bf16_f32 v191, v196, v197
	s_nop 0
	v_addc_co_u32_e32 v195, vcc, 0, v179, vcc
	global_store_dwordx4 v[194:195], v[188:191], off
	v_cvt_f32_i32_e32 v205, v3
	v_cvt_f32_i32_e32 v204, v2
	v_cvt_f32_i32_e32 v189, v17
	v_cvt_f32_i32_e32 v191, v15
	v_cvt_f32_i32_e32 v190, v14
	v_cvt_f32_i32_e32 v188, v16
	v_pk_mul_f32 v[196:197], v[210:211], v[184:185] op_sel_hi:[1,0]
	v_cvt_f32_i32_e32 v211, v13
	v_pk_mul_f32 v[190:191], v[156:157], v[190:191] op_sel_hi:[0,1]
	v_pk_mul_f32 v[188:189], v[156:157], v[188:189] op_sel_hi:[0,1]
	v_pk_mul_f32 v[198:199], v[188:189], v[188:189]
	v_pk_mul_f32 v[200:201], v[190:191], v[190:191]
	v_cvt_f32_i32_e32 v210, v12
	v_pk_mov_b32 v[202:203], v[200:201], v[198:199] op_sel:[1,0]
	v_mov_b32_e32 v201, v199
	v_cvt_f32_i32_e32 v199, v5
	v_cvt_f32_i32_e32 v198, v4
	v_pk_add_f32 v[200:201], v[202:203], v[200:201]
	v_pk_mul_f32 v[202:203], v[156:157], v[204:205] op_sel_hi:[0,1]
	v_pk_mul_f32 v[206:207], v[202:203], v[202:203]
	v_pk_mul_f32 v[198:199], v[156:157], v[198:199] op_sel_hi:[0,1]
	v_pk_mul_f32 v[204:205], v[198:199], v[198:199]
	v_pk_mul_f32 v[194:195], v[212:213], v[184:185] op_sel_hi:[1,0]
	v_pk_mov_b32 v[208:209], v[206:207], v[204:205] op_sel:[1,0]
	v_mov_b32_e32 v207, v205
	v_cvt_f32_i32_e32 v205, v11
	v_cvt_f32_i32_e32 v204, v10
	v_cvt_f32_i32_e32 v213, v7
	v_cvt_f32_i32_e32 v215, v9
	v_cvt_f32_i32_e32 v214, v8
	v_cvt_f32_i32_e32 v212, v6
	v_pk_add_f32 v[200:201], v[200:201], v[200:201] op_sel_hi:[0,1]
	v_pk_mul_f32 v[204:205], v[156:157], v[204:205] op_sel_hi:[0,1]
	v_pk_add_f32 v[206:207], v[208:209], v[206:207]
	v_pk_mul_f32 v[208:209], v[156:157], v[210:211] op_sel_hi:[0,1]
	v_mul_f32_e32 v200, v204, v204
	v_pk_fma_f32 v[210:211], v[204:205], v[204:205], v[200:201] op_sel_hi:[1,1,0]
	v_mul_f32_e32 v200, v208, v208
	v_pk_add_f32 v[206:207], v[206:207], v[206:207] op_sel_hi:[0,1]
	v_pk_fma_f32 v[216:217], v[208:209], v[208:209], v[200:201] op_sel_hi:[1,1,0]
	v_pk_mul_f32 v[214:215], v[156:157], v[214:215] op_sel_hi:[0,1]
	v_pk_mul_f32 v[212:213], v[156:157], v[212:213] op_sel_hi:[0,1]
	v_mul_f32_e32 v210, v212, v212
	v_mul_f32_e32 v216, v213, v213
	v_mul_f32_e32 v200, v214, v214
	v_mul_f32_e32 v206, v215, v215
	v_pk_add_f32 v[210:211], v[210:211], v[216:217]
	v_pk_add_f32 v[200:201], v[200:201], v[206:207]
	v_pk_mul_f32 v[186:187], v[186:187], v[184:185] op_sel_hi:[1,0]
	v_pk_add_f32 v[200:201], v[210:211], v[200:201]
	v_pk_mul_f32 v[182:183], v[182:183], v[184:185] op_sel_hi:[1,0]
	v_add_f32_e32 v163, v200, v201
	ds_bpermute_b32 v159, v159, v163
	v_pk_mul_f32 v[196:197], v[136:137], v[196:197]
	v_pk_mul_f32 v[194:195], v[134:135], v[194:195]
	v_pk_mul_f32 v[200:201], v[132:133], v[182:183]
	v_pk_mul_f32 v[184:185], v[130:131], v[186:187]
	s_waitcnt lgkmcnt(0)
	v_add_f32_e32 v159, v163, v159
	ds_bpermute_b32 v161, v161, v159
	v_cvt_pk_bf16_f32 v182, v194, v195
	v_cvt_pk_bf16_f32 v183, v196, v197
	v_cvt_pk_bf16_f32 v184, v184, v185
	v_cvt_pk_bf16_f32 v185, v200, v201
	s_waitcnt lgkmcnt(0)
	v_add_f32_e32 v159, v159, v161
	v_fmamk_f32 v159, v159, 0x3c800000, v235
	v_rsq_f32_e32 v159, v159
	global_store_dwordx4 v[180:181], v[182:185], off offset:64
	s_mov_b64 s[4:5], 0x2c000
	v_mul_f32_e32 v180, v157, v159
	v_pk_mul_f32 v[184:185], v[190:191], v[180:181] op_sel_hi:[1,0]
	v_pk_mul_f32 v[186:187], v[188:189], v[180:181] op_sel_hi:[1,0]
	v_lshl_add_u64 v[182:183], v[178:179], 0, s[4:5]
	v_pk_mul_f32 v[144:145], v[144:145], v[186:187]
	v_pk_mul_f32 v[142:143], v[142:143], v[184:185]
	v_pk_mul_f32 v[184:185], v[202:203], v[180:181] op_sel_hi:[1,0]
	v_pk_mul_f32 v[186:187], v[198:199], v[180:181] op_sel_hi:[1,0]
	s_mov_b32 s4, 0x2c000
	v_pk_mul_f32 v[186:187], v[140:141], v[186:187]
	v_pk_mul_f32 v[140:141], v[138:139], v[184:185]
	v_cvt_pk_bf16_f32 v138, v142, v143
	v_add_co_u32_e32 v142, vcc, s4, v178
	v_cvt_pk_bf16_f32 v139, v144, v145
	v_cvt_pk_bf16_f32 v140, v140, v141
	v_cvt_pk_bf16_f32 v141, v186, v187
	v_addc_co_u32_e32 v143, vcc, 0, v179, vcc
	global_store_dwordx4 v[142:143], v[138:141], off
	s_nop 1
	v_pk_mul_f32 v[138:139], v[204:205], v[180:181] op_sel_hi:[1,0]
	v_pk_mul_f32 v[140:141], v[208:209], v[180:181] op_sel_hi:[1,0]
	v_pk_mul_f32 v[134:135], v[134:135], v[138:139]
	v_pk_mul_f32 v[136:137], v[136:137], v[140:141]
	v_pk_mul_f32 v[138:139], v[212:213], v[180:181] op_sel_hi:[1,0]
	v_pk_mul_f32 v[140:141], v[214:215], v[180:181] op_sel_hi:[1,0]
	s_nop 0
	v_pk_mul_f32 v[140:141], v[132:133], v[140:141]
	v_pk_mul_f32 v[132:133], v[130:131], v[138:139]
	v_cvt_pk_bf16_f32 v130, v134, v135
	v_cvt_pk_bf16_f32 v131, v136, v137
	v_cvt_pk_bf16_f32 v132, v132, v133
	v_cvt_pk_bf16_f32 v133, v140, v141
	global_store_dwordx4 v[182:183], v[130:133], off offset:64
